# N2+ROUTER(0): the 16 workgroups that run two router tasks skip the conversion drain; the other 240 share it (stride 1920 waves)
# speedup vs baseline: 1.0083x; 1.0083x over previous
.LBB0_1058:
	s_add_i32 s1, s40, 0xffffff78
	s_lshl_b32 s0, s38, 3
	s_max_i32 s1, s1, 0
	s_mulk_i32 s1, 0x48
	s_add_i32 s0, s42, s0
	s_add_i32 s43, s0, s1
	s_addk_i32 s43, 0xff80
	s_cmp_lt_u32 s38, 16
	s_cselect_b32 s43, 0x6000, s43
	s_cmpk_gt_i32 s43, 0x5fff
	s_mov_b32 s1, 0
	s_cbranch_scc1 .LBB0_1135
	s_lshl_b32 s44, s40, 3
	s_addk_i32 s44, 0xff80
	s_add_u32 s45, s10, 0x17458000
	s_mul_i32 s0, s42, 0x2400
	s_addc_u32 s46, s11, 0
	s_add_i32 s0, s0, 0
	s_add_u32 s47, s10, 0x7458000
	s_addc_u32 s48, s11, 0
	s_add_u32 s49, s10, 0x6458000
	s_addc_u32 s50, s11, 0
	s_add_u32 s51, s10, 0x5458000
	s_addc_u32 s52, s11, 0
	s_add_u32 s53, s10, 0x4d58000
	s_addc_u32 s54, s11, 0
	s_add_u32 s55, s10, 0x158000
	s_addc_u32 s56, s11, 0
	s_add_u32 s57, s10, 0x3390c000
	s_addc_u32 s58, s11, 0
	s_add_u32 s59, s10, 0x35e0c000
	v_lshlrev_b32_e32 v2, 1, v86
	v_and_b32_e32 v0, 60, v0
	v_and_b32_e32 v80, 48, v54
	s_addc_u32 s60, s11, 0
	v_and_b32_e32 v2, 0x60, v2
	v_and_b32_e32 v8, 7, v85
	v_lshrrev_b32_e32 v90, 3, v86
	v_mov_b32_e32 v79, 0
	v_add_u32_e32 v1, s0, v76
	v_mul_u32_u24_e32 v3, 0x50, v0
	v_add_u32_e32 v4, s0, v80
	v_mul_u32_u24_e32 v5, 0x50, v87
	s_add_u32 s61, s10, 0x3760c000
	v_add_u32_e32 v6, s0, v2
	v_mul_u32_u24_e32 v7, 0x90, v0
	v_lshlrev_b32_e32 v2, 3, v8
	v_lshl_add_u32 v8, v8, 4, s0
	v_mul_u32_u24_e32 v9, 0x90, v90
	v_mov_b32_e32 v81, v79
	v_or_b32_e32 v77, 16, v87
	v_or_b32_e32 v88, 32, v87
	v_or_b32_e32 v89, 48, v87
	s_addc_u32 s62, s11, 0
	v_or_b32_e32 v91, 8, v90
	v_or_b32_e32 v92, 16, v90
	v_or_b32_e32 v93, 24, v90
	v_or_b32_e32 v94, 32, v90
	v_or_b32_e32 v95, 40, v90
	v_or_b32_e32 v96, 48, v90
	v_or_b32_e32 v97, 56, v90
	s_add_i32 s63, 0, 0x204f8
	s_movk_i32 s64, 0x2000
	s_movk_i32 s65, 0x4000
	s_movk_i32 s66, 0x6000
	s_mov_b32 s67, 0x12000
	s_mov_b32 s68, 0xc3e00000
	v_add_u32_e32 v98, v1, v3
	v_add_u32_e32 v99, v4, v5
	s_movk_i32 s69, 0x3000
	s_movk_i32 s70, 0x5000
	s_movk_i32 s71, 0x7000
	s_add_i32 s72, 0, 0x204c0
	s_add_i32 s73, 0, 0x204b8
	s_add_i32 s74, 0, 0x204b0
	s_add_i32 s75, 0, 0x204a8
	s_add_i32 s76, 0, 0x20458
	s_add_i32 s77, 0, 0x20448
	s_add_i32 s78, 0, 0x20440
	s_mov_b32 s79, 0x9000
	s_mov_b32 s80, 0x1b000
	s_mov_b32 s81, 0x25000
	s_mov_b32 s82, 0x2e000
	s_mov_b32 s83, 0x37000
	s_mov_b32 s84, 0x41000
	s_mov_b32 s85, 0x4a000
	s_mov_b32 s86, 0x53000
	s_mov_b32 s87, 0x5d000
	s_mov_b32 s88, 0x66000
	s_mov_b32 s89, 0x6f000
	s_mov_b32 s90, 0x79000
	s_mov_b32 s91, 0x82000
	s_mov_b32 s92, 0x8b000
	v_add_u32_e32 v100, v6, v7
	v_lshlrev_b32_e32 v78, 1, v2
	v_lshlrev_b32_e32 v82, 2, v0
	v_mov_b32_e32 v101, 0x43e00000
	v_mov_b32_e32 v104, v79
	v_mov_b32_e32 v105, v79
	v_mov_b32_e32 v106, v79
	v_mov_b32_e32 v107, v79
	v_add_u32_e32 v102, v8, v9
	s_branch .LBB0_1062
